# prologue: S5 table tasks dealt one per workgroup, S5 discretisation moved to workgroups 248-255, weight transposes issued as two load batches
# speedup vs baseline: 1.0055x; 1.0055x over previous
;     const size_t total = (size_t)N * (K / 8);
; #pragma unroll 1
;     for (size_t i = (size_t)bid * NTHR + threadIdx.x; i < total; i += (size_t)nb * NTHR) {
;         const int n = (int)(i % N), kc = (int)(i / N);
;         float v[8];
; #pragma unroll
;         for (int j = 0; j < 8; ++j) v[j] = W[(size_t)(kc * 8 + j) * N + n];
;         uint4 r; r.x = pack2(v[0], v[1]); r.y = pack2(v[2], v[3]); r.z = pack2(v[4], v[5]); r.w = pack2(v[6], v[7]);
;         if (FRAG) *(uint4*)&WT[((size_t)((kc >> 1) * (N / 32) + (n >> 5)) * 64 + (n & 31) + 32 * (kc & 1)) * 8] = r;
;         else *(uint4*)&WT[(size_t)n * K + kc * 8] = r;
;     }
;     ...
;     transpose_cvt(P.in[10], 1024, 3072, (bfr*)(P.ws + WS_WINT0), bid, nb);
;     transpose_cvt(P.in[11], 1024, 1024, (bfr*)(P.ws + WS_WOUTT0), bid, nb);
;     transpose_cvt(P.in[22], 1024, 1280, (bfr*)(P.ws + WS_WINT1), bid, nb);
;     transpose_cvt(P.in[23], 1024, 1024, (bfr*)(P.ws + WS_WOUTT1), bid, nb);
;     transpose_cvt<1>(P.in[36], 1024, 256, (bfr*)(P.ws + WS_ROUT), bid, nb);
;     transpose_cvt<1>(P.in[36] + 1024 * 256, 1024, 256, (bfr*)(P.ws + WS_ROUT) + 256 * 1024, bid, nb);
;     transpose_cvt(P.in[34], 512, 512, (bfr*)(P.ws + WS_GLUT), bid, nb);
.LBB0_15:
	v_readlane_b32 s0, v253, 10
	s_cmpk_lg_u32 s0, 0x100
	s_cbranch_scc1 .Ltr_orig
	s_mov_b32 s1, 0
	s_mov_b32 s45, 0
	v_writelane_b32 v253, s1, 11
	v_and_b32_e32 v66, 0xff, v0
	v_and_b32_e32 v64, 31, v0
	v_lshl_or_b32 v2, s44, 9, v0
	v_readlane_b32 s4, v253, 39
	v_readlane_b32 s5, v253, 40
	v_readlane_b32 s6, v253, 41
	v_readlane_b32 s7, v253, 42
	v_readlane_b32 s8, v253, 63
	v_readlane_b32 s9, v252, 0
	v_readlane_b32 s10, v252, 1
	v_readlane_b32 s11, v252, 2
	v_readlane_b32 s12, v252, 11
	v_readlane_b32 s13, v252, 12
	v_readlane_b32 s16, v252, 7
	v_readlane_b32 s17, v252, 8
	s_mov_b32 s2, 0xaaaaaaab
	s_mov_b32 s3, 0xcccccccd
	s_mov_b32 s20, 0x18000
	s_mov_b32 s21, 0xa000
	v_mov_b32_e32 v23, v2
	v_mul_hi_u32 v24, v23, s2
	v_lshrrev_b32_e32 v24, 11, v24
	v_mul_u32_u24_e32 v25, 0xc00, v24
	v_sub_u32_e32 v25, v23, v25
	v_mul_lo_u32 v3, v24, s20
	v_lshl_add_u32 v3, v25, 2, v3
	v_lshlrev_b32_e32 v25, 11, v25
	v_lshl_add_u32 v12, v24, 4, v25
	v_add_u32_e32 v12, 0x28000, v12
	v_add_u32_e32 v23, 0x20000, v2
	v_mul_hi_u32 v24, v23, s2
	v_lshrrev_b32_e32 v24, 11, v24
	v_mul_u32_u24_e32 v25, 0xc00, v24
	v_sub_u32_e32 v25, v23, v25
	v_mul_lo_u32 v4, v24, s20
	v_lshl_add_u32 v4, v25, 2, v4
	v_lshlrev_b32_e32 v25, 11, v25
	v_lshl_add_u32 v13, v24, 4, v25
	v_add_u32_e32 v13, 0x28000, v13
	v_add_u32_e32 v23, 0x40000, v2
	v_mul_hi_u32 v24, v23, s2
	v_lshrrev_b32_e32 v24, 11, v24
	v_mul_u32_u24_e32 v25, 0xc00, v24
	v_sub_u32_e32 v25, v23, v25
	v_mul_lo_u32 v5, v24, s20
	v_lshl_add_u32 v5, v25, 2, v5
	v_lshlrev_b32_e32 v25, 11, v25
	v_lshl_add_u32 v14, v24, 4, v25
	v_add_u32_e32 v14, 0x28000, v14
	v_lshrrev_b32_e32 v24, 10, v2
	v_and_b32_e32 v25, 0x3ff, v2
	v_lshlrev_b32_e32 v6, 15, v24
	v_lshl_add_u32 v6, v25, 2, v6
	v_mov_b32_e32 v8, v6
	v_lshlrev_b32_e32 v25, 11, v25
	v_lshl_add_u32 v15, v24, 4, v25
	v_add_u32_e32 v17, 0xaa8000, v15
	v_add_u32_e32 v15, 0x628000, v15
	v_mov_b32_e32 v23, v2
	v_mul_hi_u32 v24, v23, s3
	v_lshrrev_b32_e32 v24, 10, v24
	v_mul_u32_u24_e32 v25, 0x500, v24
	v_sub_u32_e32 v25, v23, v25
	v_mul_lo_u32 v7, v24, s21
	v_lshl_add_u32 v7, v25, 2, v7
	v_lshlrev_b32_e32 v25, 11, v25
	v_lshl_add_u32 v16, v24, 4, v25
	v_add_u32_e32 v16, 0x828000, v16
	v_add_u32_e32 v23, 0x20000, v2
	v_mul_hi_u32 v24, v23, s3
	v_lshrrev_b32_e32 v24, 10, v24
	v_mul_u32_u24_e32 v25, 0x500, v24
	v_sub_u32_e32 v25, v23, v25
	v_mul_lo_u32 v9, v24, s21
	v_lshl_add_u32 v9, v25, 2, v9
	v_lshlrev_b32_e32 v25, 11, v25
	v_lshl_add_u32 v18, v24, 4, v25
	v_add_u32_e32 v18, 0x828000, v18
	v_lshrrev_b32_e32 v24, 8, v2
	v_lshlrev_b32_e32 v10, 13, v24
	v_lshl_add_u32 v10, v66, 2, v10
	v_lshrrev_b32_e32 v24, 6, v2
	v_and_b32_e32 v24, 0x1f8, v24
	v_bfe_u32 v25, v2, 5, 3
	v_or_b32_e32 v24, v24, v25
	v_lshrrev_b32_e32 v25, 3, v2
	v_and_b32_e32 v25, 32, v25
	v_lshlrev_b32_e32 v24, 6, v24
	v_or3_b32 v24, v24, v25, v64
	v_lshlrev_b32_e32 v24, 4, v24
	v_add_u32_e32 v19, 0xca8000, v24
	v_add_u32_e32 v20, 0xd28000, v24
	v_lshlrev_b32_e32 v11, 2, v0
	v_mov_b32_e32 v24, s44
	v_lshl_add_u32 v11, v24, 14, v11
	v_lshlrev_b32_e32 v21, 10, v0
	v_lshl_add_u32 v21, v24, 4, v21
	v_add_u32_e32 v21, 0xda8000, v21
	v_readlane_b32 s18, v253, 63
	v_readlane_b32 s19, v252, 0
	s_add_u32 s14, s12, 0x100000
	s_addc_u32 s15, s13, 0
	global_load_dword v70, v3, s[4:5]
	global_load_dword v78, v4, s[4:5]
	global_load_dword v86, v5, s[4:5]
	global_load_dword v94, v6, s[6:7]
	s_add_u32 s4, s4, 0x3000
	s_addc_u32 s5, s5, 0
	s_add_u32 s6, s6, 0x1000
	s_addc_u32 s7, s7, 0
	global_load_dword v71, v3, s[4:5]
	global_load_dword v79, v4, s[4:5]
	global_load_dword v87, v5, s[4:5]
	global_load_dword v95, v6, s[6:7]
	s_add_u32 s4, s4, 0x3000
	s_addc_u32 s5, s5, 0
	s_add_u32 s6, s6, 0x1000
	s_addc_u32 s7, s7, 0
	global_load_dword v72, v3, s[4:5]
	global_load_dword v80, v4, s[4:5]
	global_load_dword v88, v5, s[4:5]
	global_load_dword v96, v6, s[6:7]
	s_add_u32 s4, s4, 0x3000
	s_addc_u32 s5, s5, 0
	s_add_u32 s6, s6, 0x1000
	s_addc_u32 s7, s7, 0
	global_load_dword v73, v3, s[4:5]
	global_load_dword v81, v4, s[4:5]
	global_load_dword v89, v5, s[4:5]
	global_load_dword v97, v6, s[6:7]
	s_add_u32 s4, s4, 0x3000
	s_addc_u32 s5, s5, 0
	s_add_u32 s6, s6, 0x1000
	s_addc_u32 s7, s7, 0
	global_load_dword v74, v3, s[4:5]
	global_load_dword v82, v4, s[4:5]
	global_load_dword v90, v5, s[4:5]
	global_load_dword v98, v6, s[6:7]
	s_add_u32 s4, s4, 0x3000
	s_addc_u32 s5, s5, 0
	s_add_u32 s6, s6, 0x1000
	s_addc_u32 s7, s7, 0
	global_load_dword v75, v3, s[4:5]
	global_load_dword v83, v4, s[4:5]
	global_load_dword v91, v5, s[4:5]
	global_load_dword v99, v6, s[6:7]
	s_add_u32 s4, s4, 0x3000
	s_addc_u32 s5, s5, 0
	s_add_u32 s6, s6, 0x1000
	s_addc_u32 s7, s7, 0
	global_load_dword v76, v3, s[4:5]
	global_load_dword v84, v4, s[4:5]
	global_load_dword v92, v5, s[4:5]
	global_load_dword v100, v6, s[6:7]
	s_add_u32 s4, s4, 0x3000
	s_addc_u32 s5, s5, 0
	s_add_u32 s6, s6, 0x1000
	s_addc_u32 s7, s7, 0
	global_load_dword v77, v3, s[4:5]
	global_load_dword v85, v4, s[4:5]
	global_load_dword v93, v5, s[4:5]
	global_load_dword v101, v6, s[6:7]
	global_load_dword v102, v7, s[8:9]
	global_load_dword v110, v8, s[10:11]
	s_add_u32 s8, s8, 0x1400
	s_addc_u32 s9, s9, 0
	s_add_u32 s10, s10, 0x1000
	s_addc_u32 s11, s11, 0
	global_load_dword v103, v7, s[8:9]
	global_load_dword v111, v8, s[10:11]
	s_add_u32 s8, s8, 0x1400
	s_addc_u32 s9, s9, 0
	s_add_u32 s10, s10, 0x1000
	s_addc_u32 s11, s11, 0
	global_load_dword v104, v7, s[8:9]
	global_load_dword v112, v8, s[10:11]
	s_add_u32 s8, s8, 0x1400
	s_addc_u32 s9, s9, 0
	s_add_u32 s10, s10, 0x1000
	s_addc_u32 s11, s11, 0
	global_load_dword v105, v7, s[8:9]
	global_load_dword v113, v8, s[10:11]
	s_add_u32 s8, s8, 0x1400
	s_addc_u32 s9, s9, 0
	s_add_u32 s10, s10, 0x1000
	s_addc_u32 s11, s11, 0
	global_load_dword v106, v7, s[8:9]
	global_load_dword v114, v8, s[10:11]
	s_add_u32 s8, s8, 0x1400
	s_addc_u32 s9, s9, 0
	s_add_u32 s10, s10, 0x1000
	s_addc_u32 s11, s11, 0
	global_load_dword v107, v7, s[8:9]
	global_load_dword v115, v8, s[10:11]
	s_add_u32 s8, s8, 0x1400
	s_addc_u32 s9, s9, 0
	s_add_u32 s10, s10, 0x1000
	s_addc_u32 s11, s11, 0
	global_load_dword v108, v7, s[8:9]
	global_load_dword v116, v8, s[10:11]
	s_add_u32 s8, s8, 0x1400
	s_addc_u32 s9, s9, 0
	s_add_u32 s10, s10, 0x1000
	s_addc_u32 s11, s11, 0
	global_load_dword v109, v7, s[8:9]
	global_load_dword v117, v8, s[10:11]
	s_cmp_lt_u32 s44, 64
	s_cbranch_scc0 .Ltr_pathb
;     const size_t total = (size_t)N * (K / 8);
; #pragma unroll 1
;     for (size_t i = (size_t)bid * NTHR + threadIdx.x; i < total; i += (size_t)nb * NTHR) {
;         const int n = (int)(i % N), kc = (int)(i / N);
;         float v[8];
; #pragma unroll
;         for (int j = 0; j < 8; ++j) v[j] = W[(size_t)(kc * 8 + j) * N + n];
;         uint4 r; r.x = pack2(v[0], v[1]); r.y = pack2(v[2], v[3]); r.z = pack2(v[4], v[5]); r.w = pack2(v[6], v[7]);
;         if (FRAG) *(uint4*)&WT[((size_t)((kc >> 1) * (N / 32) + (n >> 5)) * 64 + (n & 31) + 32 * (kc & 1)) * 8] = r;
;         else *(uint4*)&WT[(size_t)n * K + kc * 8] = r;
;     }
;     ...
;     transpose_cvt(P.in[22], 1024, 1280, (bfr*)(P.ws + WS_WINT1), bid, nb);
;     transpose_cvt(P.in[23], 1024, 1024, (bfr*)(P.ws + WS_WOUTT1), bid, nb);
;     transpose_cvt<1>(P.in[36], 1024, 256, (bfr*)(P.ws + WS_ROUT), bid, nb);
;     transpose_cvt<1>(P.in[36] + 1024 * 256, 1024, 256, (bfr*)(P.ws + WS_ROUT) + 256 * 1024, bid, nb);
;     transpose_cvt(P.in[34], 512, 512, (bfr*)(P.ws + WS_GLUT), bid, nb);
	s_waitcnt vmcnt(16)
	v_cvt_pk_bf16_f32 v70, v70, v71
	v_cvt_pk_bf16_f32 v71, v72, v73
	v_cvt_pk_bf16_f32 v72, v74, v75
	v_cvt_pk_bf16_f32 v73, v76, v77
	global_store_dwordx4 v12, v[70:73], s[42:43]
	v_cvt_pk_bf16_f32 v78, v78, v79
	v_cvt_pk_bf16_f32 v79, v80, v81
	v_cvt_pk_bf16_f32 v80, v82, v83
	v_cvt_pk_bf16_f32 v81, v84, v85
	global_store_dwordx4 v13, v[78:81], s[42:43]
	v_cvt_pk_bf16_f32 v86, v86, v87
	v_cvt_pk_bf16_f32 v87, v88, v89
	v_cvt_pk_bf16_f32 v88, v90, v91
	v_cvt_pk_bf16_f32 v89, v92, v93
	global_store_dwordx4 v14, v[86:89], s[42:43]
	v_cvt_pk_bf16_f32 v94, v94, v95
	v_cvt_pk_bf16_f32 v95, v96, v97
	v_cvt_pk_bf16_f32 v96, v98, v99
	v_cvt_pk_bf16_f32 v97, v100, v101
	global_store_dwordx4 v15, v[94:97], s[42:43]
	global_load_dword v118, v9, s[18:19]
	global_load_dword v126, v10, s[12:13]
	global_load_dword v134, v10, s[14:15]
	global_load_dword v142, v11, s[16:17]
	s_add_u32 s18, s18, 0x1400
	s_addc_u32 s19, s19, 0
	s_add_u32 s12, s12, 0x400
	s_addc_u32 s13, s13, 0
	s_add_u32 s14, s14, 0x400
	s_addc_u32 s15, s15, 0
	s_add_u32 s16, s16, 0x800
	s_addc_u32 s17, s17, 0
	global_load_dword v119, v9, s[18:19]
	global_load_dword v127, v10, s[12:13]
	global_load_dword v135, v10, s[14:15]
	global_load_dword v143, v11, s[16:17]
	s_add_u32 s18, s18, 0x1400
	s_addc_u32 s19, s19, 0
	s_add_u32 s12, s12, 0x400
	s_addc_u32 s13, s13, 0
	s_add_u32 s14, s14, 0x400
	s_addc_u32 s15, s15, 0
	s_add_u32 s16, s16, 0x800
	s_addc_u32 s17, s17, 0
	global_load_dword v120, v9, s[18:19]
	global_load_dword v128, v10, s[12:13]
	global_load_dword v136, v10, s[14:15]
	global_load_dword v144, v11, s[16:17]
	s_add_u32 s18, s18, 0x1400
	s_addc_u32 s19, s19, 0
	s_add_u32 s12, s12, 0x400
	s_addc_u32 s13, s13, 0
	s_add_u32 s14, s14, 0x400
	s_addc_u32 s15, s15, 0
	s_add_u32 s16, s16, 0x800
	s_addc_u32 s17, s17, 0
	global_load_dword v121, v9, s[18:19]
	global_load_dword v129, v10, s[12:13]
	global_load_dword v137, v10, s[14:15]
	global_load_dword v145, v11, s[16:17]
	s_add_u32 s18, s18, 0x1400
	s_addc_u32 s19, s19, 0
	s_add_u32 s12, s12, 0x400
	s_addc_u32 s13, s13, 0
	s_add_u32 s14, s14, 0x400
	s_addc_u32 s15, s15, 0
	s_add_u32 s16, s16, 0x800
	s_addc_u32 s17, s17, 0
	global_load_dword v122, v9, s[18:19]
	global_load_dword v130, v10, s[12:13]
	global_load_dword v138, v10, s[14:15]
	global_load_dword v146, v11, s[16:17]
	s_add_u32 s18, s18, 0x1400
	s_addc_u32 s19, s19, 0
	s_add_u32 s12, s12, 0x400
	s_addc_u32 s13, s13, 0
	s_add_u32 s14, s14, 0x400
	s_addc_u32 s15, s15, 0
	s_add_u32 s16, s16, 0x800
	s_addc_u32 s17, s17, 0
	global_load_dword v123, v9, s[18:19]
	global_load_dword v131, v10, s[12:13]
	global_load_dword v139, v10, s[14:15]
	global_load_dword v147, v11, s[16:17]
	s_add_u32 s18, s18, 0x1400
	s_addc_u32 s19, s19, 0
	s_add_u32 s12, s12, 0x400
	s_addc_u32 s13, s13, 0
	s_add_u32 s14, s14, 0x400
	s_addc_u32 s15, s15, 0
	s_add_u32 s16, s16, 0x800
	s_addc_u32 s17, s17, 0
	global_load_dword v124, v9, s[18:19]
	global_load_dword v132, v10, s[12:13]
	global_load_dword v140, v10, s[14:15]
	global_load_dword v148, v11, s[16:17]
	s_add_u32 s18, s18, 0x1400
	s_addc_u32 s19, s19, 0
	s_add_u32 s12, s12, 0x400
	s_addc_u32 s13, s13, 0
	s_add_u32 s14, s14, 0x400
	s_addc_u32 s15, s15, 0
	s_add_u32 s16, s16, 0x800
	s_addc_u32 s17, s17, 0
	global_load_dword v125, v9, s[18:19]
	global_load_dword v133, v10, s[12:13]
	global_load_dword v141, v10, s[14:15]
	global_load_dword v149, v11, s[16:17]
	s_waitcnt vmcnt(36)
	v_cvt_pk_bf16_f32 v102, v102, v103
	v_cvt_pk_bf16_f32 v103, v104, v105
	v_cvt_pk_bf16_f32 v104, v106, v107
	v_cvt_pk_bf16_f32 v105, v108, v109
	global_store_dwordx4 v16, v[102:105], s[42:43]
	v_cvt_pk_bf16_f32 v110, v110, v111
	v_cvt_pk_bf16_f32 v111, v112, v113
	v_cvt_pk_bf16_f32 v112, v114, v115
	v_cvt_pk_bf16_f32 v113, v116, v117
	global_store_dwordx4 v17, v[110:113], s[42:43]
	s_waitcnt vmcnt(2)
	v_cvt_pk_bf16_f32 v118, v118, v119
	v_cvt_pk_bf16_f32 v119, v120, v121
	v_cvt_pk_bf16_f32 v120, v122, v123
	v_cvt_pk_bf16_f32 v121, v124, v125
	global_store_dwordx4 v18, v[118:121], s[42:43]
	v_cvt_pk_bf16_f32 v126, v126, v127
	v_cvt_pk_bf16_f32 v127, v128, v129
	v_cvt_pk_bf16_f32 v128, v130, v131
	v_cvt_pk_bf16_f32 v129, v132, v133
	global_store_dwordx4 v19, v[126:129], s[42:43]
	v_cvt_pk_bf16_f32 v134, v134, v135
	v_cvt_pk_bf16_f32 v135, v136, v137
	v_cvt_pk_bf16_f32 v136, v138, v139
	v_cvt_pk_bf16_f32 v137, v140, v141
	global_store_dwordx4 v20, v[134:137], s[42:43]
	v_cvt_pk_bf16_f32 v142, v142, v143
	v_cvt_pk_bf16_f32 v143, v144, v145
	v_cvt_pk_bf16_f32 v144, v146, v147
	v_cvt_pk_bf16_f32 v145, v148, v149
	global_store_dwordx4 v21, v[142:145], s[42:43]
	s_branch .Ltr_done
.Ltr_pathb:
	s_waitcnt vmcnt(16)
	v_cvt_pk_bf16_f32 v70, v70, v71
	v_cvt_pk_bf16_f32 v71, v72, v73
	v_cvt_pk_bf16_f32 v72, v74, v75
	v_cvt_pk_bf16_f32 v73, v76, v77
	global_store_dwordx4 v12, v[70:73], s[42:43]
	v_cvt_pk_bf16_f32 v78, v78, v79
	v_cvt_pk_bf16_f32 v79, v80, v81
	v_cvt_pk_bf16_f32 v80, v82, v83
	v_cvt_pk_bf16_f32 v81, v84, v85
	global_store_dwordx4 v13, v[78:81], s[42:43]
	v_cvt_pk_bf16_f32 v86, v86, v87
	v_cvt_pk_bf16_f32 v87, v88, v89
	v_cvt_pk_bf16_f32 v88, v90, v91
	v_cvt_pk_bf16_f32 v89, v92, v93
	global_store_dwordx4 v14, v[86:89], s[42:43]
	v_cvt_pk_bf16_f32 v94, v94, v95
	v_cvt_pk_bf16_f32 v95, v96, v97
	v_cvt_pk_bf16_f32 v96, v98, v99
	v_cvt_pk_bf16_f32 v97, v100, v101
	global_store_dwordx4 v15, v[94:97], s[42:43]
	s_waitcnt vmcnt(4)
	v_cvt_pk_bf16_f32 v102, v102, v103
	v_cvt_pk_bf16_f32 v103, v104, v105
	v_cvt_pk_bf16_f32 v104, v106, v107
	v_cvt_pk_bf16_f32 v105, v108, v109
	global_store_dwordx4 v16, v[102:105], s[42:43]
	v_cvt_pk_bf16_f32 v110, v110, v111
	v_cvt_pk_bf16_f32 v111, v112, v113
	v_cvt_pk_bf16_f32 v112, v114, v115
	v_cvt_pk_bf16_f32 v113, v116, v117
	global_store_dwordx4 v17, v[110:113], s[42:43]
	s_branch .Ltr_done

;     ...
;     const float* w1 = P.in[15]; const float* b1 = P.in[16]; const float* fq = P.in[17];
;     const float* w2 = P.in[18]; const float* b2 = P.in[19]; const float* w3 = P.in[20];
;     float* zemb = sm;
;     float* h1 = sm + 32 * 33;
;     float* h2 = h1 + 32 * 64;
;     const int tid = threadIdx.x;
;     __syncthreads();
;     for (int e = tid; e < 32 * 33; e += NTHR) {
;         const int pp = e / 33, i = e % 33;
;         const float pos = (float)(p0 + pp);
;         float v;
;         if (i == 0) v = pos / (float)(l - 1);
;         else {
;             const int b = (i - 1) & 15;
;             const float band = 1e-4f + (float)b * ((15.f - 1e-4f) / 15.f);
;             const float ang = ((float)(2.0 * 3.14159265358979323846 / (double)l) * pos) * band;
;             v = (i <= 16) ? cosf(ang) : -sinf(ang);
;         }
;         zemb[e] = v;
;     }
;     __syncthreads();
;     for (int e = tid; e < 32 * 64; e += NTHR) {
;         const int pp = e >> 6, j = e & 63;
;         float s = b1[j];
; #pragma unroll 4
;         for (int i = 0; i < 33; ++i) s += zemb[pp * 33 + i] * w1[i * 64 + j];
;         h1[e] = sinf(fq[j] * s);
;     }
;     __syncthreads();
;     for (int e = tid; e < 32 * 64; e += NTHR) {
;         const int pp = e >> 6, j = e & 63;
;         float s = b2[j];
; #pragma unroll 4
;         for (int i = 0; i < 64; ++i) s += h1[pp * 64 + i] * w2[i * 64 + j];
;         h2[e] = sinf(fq[j] * s);
;     }
;     __syncthreads();
;     const float lo = -4.605170185988091f / 1.5f, hi = -4.605170185988091f / 0.3f;
;     const float delta = fabsf(lo + (float)tid * ((hi - lo) / 511.f));
;     float* HF = isctx ? (float*)(P.ws + WS_HFC) + (size_t)tid * 512 + 256 : (float*)(P.ws + WS_HF) + (size_t)tid * 32768 + LSEQ;
.Ltr_done:
	s_cmpk_gt_i32 s44, 0x207
	s_cbranch_scc1 .LBB0_109
	v_cvt_f32_u32_e32 v2, v0
	v_readlane_b32 s12, v253, 51
	v_mul_u32_u24_e32 v3, 0x208, v0
	v_lshlrev_b32_e32 v6, 2, v202
	v_mov_b32_e32 v7, 0
	v_readlane_b32 s13, v253, 52
	v_readlane_b32 s14, v253, 53
	v_readlane_b32 s15, v253, 54
	v_readlane_b32 s18, v253, 57
	v_readlane_b32 s19, v253, 58
	v_readlane_b32 s0, v252, 19
	v_mov_b32_e32 v67, 0xc0447cbd
	v_lshl_add_u64 v[8:9], s[12:13], 0, v[6:7]
	v_lshl_add_u64 v[10:11], s[14:15], 0, v[6:7]
	v_lshl_add_u64 v[12:13], s[18:19], 0, v[6:7]
	v_lshlrev_b32_e32 v6, 2, v3
	v_readlane_b32 s1, v252, 20
	v_readlane_b32 s2, v252, 21
	v_readlane_b32 s3, v252, 22
	v_fmac_f32_e32 v67, 0xbcc4df2d, v2
	s_mov_b64 s[0:1], 0x40662400
	v_lshl_add_u64 v[2:3], s[2:3], 0, v[6:7]
	v_lshl_add_u64 v[14:15], v[2:3], 0, s[0:1]
	v_mul_u32_u24_e32 v3, 0x84, v1
	v_readlane_b32 s0, v253, 35
	v_add3_u32 v69, v3, 0, 16
	v_mov_b32_e32 v3, 0x200
	v_readlane_b32 s10, v253, 45
	v_readlane_b32 s11, v253, 46
	v_readlane_b32 s16, v253, 55
	v_readlane_b32 s17, v253, 56
	v_readlane_b32 s20, v253, 59
	v_readlane_b32 s21, v253, 60
	v_readlane_b32 s24, v253, 63
	v_readlane_b32 s25, v252, 0
	v_readlane_b32 s26, v252, 1
	v_readlane_b32 s27, v252, 2
	v_lshlrev_b32_e32 v2, 2, v0
	v_lshl_or_b32 v6, v202, 2, v3
	v_readlane_b32 s12, v253, 47
	v_readlane_b32 s13, v253, 48
	v_readlane_b32 s14, v253, 49
	v_readlane_b32 s15, v253, 50
	v_mov_b32_e32 v3, v7
	s_mov_b32 s10, 0x54442d18
	v_add3_u32 v68, v2, 0, 16
	v_lshl_add_u64 v[16:17], s[14:15], 0, v[6:7]
	v_lshl_add_u64 v[18:19], s[16:17], 0, v[6:7]
	v_lshl_add_u64 v[20:21], s[20:21], 0, v[2:3]
	s_mov_b32 s11, 0x401921fb
	v_mov_b32_e32 v23, 0x3f7fff90
	s_brev_b32 s24, 18
	s_mov_b32 s25, 0xfe5163ab
	s_mov_b32 s26, 0x3c439041
	s_mov_b32 s27, 0xdb629599
	s_mov_b32 s28, 0xf534ddc0
	s_mov_b32 s29, 0xfc2757d1
	s_mov_b32 s30, 0x4e441529
	s_mov_b32 s31, 0xa2f9836e
	s_mov_b32 s34, 0x3fc90fda
	s_mov_b32 s35, 0x3f22f983
	s_mov_b32 s36, 0xbfc90fda
	v_mov_b32_e32 v70, 0x3c0881c4
	v_mov_b32_e32 v71, 0xbab64f3b
	s_movk_i32 s37, 0x1f8
	s_mov_b64 s[12:13], 0x400
	s_movk_i32 s38, 0x5ff
	s_add_i32 s39, 0, 0x1090
	s_mov_b32 s40, 0x3fb8aa3b
	s_mov_b32 s41, 0xc2ce8ed0
	s_mov_b32 s42, 0x42b17218
	v_not_b32_e32 v72, 63
	v_not_b32_e32 v73, 31
	v_mov_b32_e32 v74, 0xffc00000
	v_mov_b32_e32 v75, 0x7fc00000
	v_mov_b32_e32 v76, 0x7f800000
	s_mov_b32 s14, s44
	v_readlane_b32 s22, v253, 61
	v_readlane_b32 s23, v253, 62
	v_readlane_b32 s1, v253, 36
	v_readlane_b32 s2, v253, 37
	v_readlane_b32 s3, v253, 38
	v_readlane_b32 s4, v253, 39
	v_readlane_b32 s5, v253, 40
	v_readlane_b32 s6, v253, 41
	v_readlane_b32 s7, v253, 42
	v_readlane_b32 s8, v253, 43
	v_readlane_b32 s9, v253, 44
	global_load_dword v104, v[16:17], off offset:-512
	global_load_dword v105, v[16:17], off offset:-256
	global_load_dword v106, v[16:17], off
	global_load_dword v107, v[16:17], off offset:256
	global_load_dword v108, v[16:17], off offset:512
	global_load_dword v109, v[16:17], off offset:768
	global_load_dword v110, v[16:17], off offset:1024
	global_load_dword v111, v[16:17], off offset:1280
	global_load_dword v112, v[16:17], off offset:1536
	global_load_dword v113, v[16:17], off offset:1792
	global_load_dword v114, v[16:17], off offset:2048
	global_load_dword v115, v[16:17], off offset:2304
	global_load_dword v116, v[16:17], off offset:2560
	global_load_dword v117, v[16:17], off offset:2816
	global_load_dword v118, v[16:17], off offset:3072
	global_load_dword v119, v[16:17], off offset:3328
	s_mov_b64 s[98:99], 0x1000
	v_lshl_add_u64 v[2:3], v[16:17], 0, s[98:99]
	global_load_dword v120, v[2:3], off offset:-512
	global_load_dword v121, v[2:3], off offset:-256
	global_load_dword v122, v[2:3], off
	global_load_dword v123, v[2:3], off offset:256
	global_load_dword v124, v[2:3], off offset:512
	global_load_dword v125, v[2:3], off offset:768
	global_load_dword v126, v[2:3], off offset:1024
;     ...
;     for (int e = tid; e < 32 * 64; e += NTHR) {
;         const int pp = e >> 6, j = e & 63;
;         float s = b1[j];
; #pragma unroll 4
;         for (int i = 0; i < 33; ++i) s += zemb[pp * 33 + i] * w1[i * 64 + j];
;         h1[e] = sinf(fq[j] * s);
;     }
;     __syncthreads();
;     for (int e = tid; e < 32 * 64; e += NTHR) {
;         const int pp = e >> 6, j = e & 63;
;         float s = b2[j];
; #pragma unroll 4
;         for (int i = 0; i < 64; ++i) s += h1[pp * 64 + i] * w2[i * 64 + j];
;         h2[e] = sinf(fq[j] * s);
	global_load_dword v127, v[2:3], off offset:1280
	global_load_dword v128, v[2:3], off offset:1536
	global_load_dword v129, v[2:3], off offset:1792
	global_load_dword v130, v[2:3], off offset:2048
	global_load_dword v131, v[2:3], off offset:2304
	global_load_dword v132, v[2:3], off offset:2560
	global_load_dword v133, v[2:3], off offset:2816
	global_load_dword v134, v[2:3], off offset:3072
	global_load_dword v135, v[2:3], off offset:3328
	s_mov_b64 s[98:99], 0x2000
	v_lshl_add_u64 v[2:3], v[16:17], 0, s[98:99]
	global_load_dword v136, v[2:3], off offset:-512
	global_load_dword v137, v[18:19], off offset:-512
	global_load_dword v138, v[18:19], off offset:-256
	global_load_dword v139, v[18:19], off
	global_load_dword v140, v[18:19], off offset:256
	global_load_dword v141, v[18:19], off offset:512
	global_load_dword v142, v[18:19], off offset:768
	global_load_dword v143, v[18:19], off offset:1024
	global_load_dword v144, v[18:19], off offset:1280
	global_load_dword v145, v[18:19], off offset:1536
	global_load_dword v146, v[18:19], off offset:1792
	global_load_dword v147, v[18:19], off offset:2048
	global_load_dword v148, v[18:19], off offset:2304
	global_load_dword v149, v[18:19], off offset:2560
	global_load_dword v150, v[18:19], off offset:2816
	global_load_dword v151, v[18:19], off offset:3072
	global_load_dword v152, v[18:19], off offset:3328
	s_mov_b64 s[98:99], 0x1000
	v_lshl_add_u64 v[2:3], v[18:19], 0, s[98:99]
	global_load_dword v153, v[2:3], off offset:-512
	global_load_dword v154, v[2:3], off offset:-256
	global_load_dword v155, v[2:3], off
	global_load_dword v156, v[2:3], off offset:256
	global_load_dword v157, v[2:3], off offset:512
	global_load_dword v158, v[2:3], off offset:768
	global_load_dword v159, v[2:3], off offset:1024
	global_load_dword v160, v[2:3], off offset:1280
	global_load_dword v161, v[2:3], off offset:1536
	global_load_dword v162, v[2:3], off offset:1792
	global_load_dword v163, v[2:3], off offset:2048
	global_load_dword v164, v[2:3], off offset:2304
	global_load_dword v165, v[2:3], off offset:2560
	global_load_dword v166, v[2:3], off offset:2816
	global_load_dword v167, v[2:3], off offset:3072
	global_load_dword v168, v[2:3], off offset:3328
	s_mov_b64 s[98:99], 0x2000
	v_lshl_add_u64 v[2:3], v[18:19], 0, s[98:99]
	global_load_dword v169, v[2:3], off offset:-512
	global_load_dword v170, v[2:3], off offset:-256
	global_load_dword v171, v[2:3], off
	global_load_dword v172, v[2:3], off offset:256
	global_load_dword v173, v[2:3], off offset:512
	global_load_dword v174, v[2:3], off offset:768
	global_load_dword v175, v[2:3], off offset:1024
	global_load_dword v176, v[2:3], off offset:1280
	global_load_dword v177, v[2:3], off offset:1536
	global_load_dword v178, v[2:3], off offset:1792
	global_load_dword v179, v[2:3], off offset:2048
	global_load_dword v180, v[2:3], off offset:2304
	global_load_dword v181, v[2:3], off offset:2560
	global_load_dword v182, v[2:3], off offset:2816
	global_load_dword v183, v[2:3], off offset:3072
	global_load_dword v184, v[2:3], off offset:3328
	s_mov_b64 s[98:99], 0x3000
	v_lshl_add_u64 v[2:3], v[18:19], 0, s[98:99]
	global_load_dword v185, v[2:3], off offset:-512
	global_load_dword v186, v[2:3], off offset:-256
	global_load_dword v187, v[2:3], off
	global_load_dword v188, v[2:3], off offset:256
	global_load_dword v189, v[2:3], off offset:512
	global_load_dword v190, v[2:3], off offset:768
	global_load_dword v191, v[2:3], off offset:1024
	global_load_dword v192, v[2:3], off offset:1280
	global_load_dword v193, v[2:3], off offset:1536
	global_load_dword v194, v[2:3], off offset:1792
	global_load_dword v195, v[2:3], off offset:2048
	global_load_dword v196, v[2:3], off offset:2304
	global_load_dword v197, v[2:3], off offset:2560
	global_load_dword v198, v[2:3], off offset:2816
	global_load_dword v199, v[2:3], off offset:3072
	global_load_dword v200, v[2:3], off offset:3328
	s_branch .LBB0_37

; __device__ __forceinline__ void s5_tables(const Params& P, float* sm, int bid, int nb) {
;     const int tid = threadIdx.x;
;     if (nb <= 8) return;
;     float2* Lam = (float2*)sm;
;     float2* Ab = Lam + 64;
;     float2* Bb = Ab + 64;
;     float2* Cc = Bb + 1024;
;     float2* W = Cc + 1024;
;     float2* Pw = W + 1024;
;     float* Kq = (float*)(Pw + 1024);
;     for (int task = bid - 8; task >= 0 && task < 256; task += nb - 8) {
;         const int dg = task & 63, q = task >> 6, dir = dg >> 5;
;         const float dt = expf(P.in[28][dg]);
;         __syncthreads();
.LBB0_109:
	v_readlane_b32 s0, v253, 10
	s_mov_b32 s4, s0
	s_cmp_lt_i32 s0, 9
	s_mov_b32 s72, s44
	v_readlane_b32 s1, v253, 11
	s_cbranch_scc1 .LBB0_280
	s_add_i32 s28, s44, -8
	s_cmp_lt_i32 s28, 0
	s_cselect_b32 s29, s0, 0
	s_add_i32 s28, s28, s29
	s_cmpk_gt_u32 s28, 0xff
	s_cbranch_scc1 .LBB0_279
	s_movk_i32 s0, 0xff
	v_or_b32_e32 v2, 0x200, v0
	v_cmp_lt_u32_e64 s[8:9], s0, v0
	s_movk_i32 s0, 0x100
	v_lshrrev_b32_e32 v3, 4, v0
	v_cmp_gt_u32_e64 s[10:11], s0, v0
	v_readlane_b32 s0, v253, 10
	v_lshl_add_u32 v34, v3, 3, 0
	v_lshrrev_b32_e32 v3, 1, v2
	v_readlane_b32 s12, v252, 19
	v_readlane_b32 s1, v253, 11
	v_and_b32_e32 v3, 0x1f8, v3
	v_lshrrev_b32_e32 v36, 6, v2
	v_add_u32_e32 v2, 0, v65
	v_lshlrev_b32_e32 v10, 4, v0
	v_mov_b32_e32 v11, 0
	v_readlane_b32 s14, v252, 21
	v_readlane_b32 s15, v252, 22
	s_mov_b32 s4, s0
	s_mov_b32 s29, s0
	v_add_u32_e32 v35, 0, v3
	v_add_u32_e32 v37, 0x2410, v2
	s_mov_b32 s34, s0
	v_lshl_add_u64 v[2:3], s[14:15], 0, v[10:11]
	s_mov_b64 s[0:1], 0x40766408
	v_lshl_add_u64 v[12:13], v[2:3], 0, s[0:1]
	s_lshl_b32 s0, s72, 9
	s_lshl_b32 s35, s28, 9
	s_mov_b64 s[0:1], 0x41b66408
	v_lshl_add_u64 v[14:15], v[2:3], 0, s[0:1]
	v_lshlrev_b32_e32 v5, 5, v0
	v_and_b32_e32 v6, 0x100, v0
	s_movk_i32 s0, 0x1e00
	v_and_or_b32 v5, v5, s0, v6
	v_and_b32_e32 v4, 15, v0
	v_add_u32_e32 v5, 0, v5
	v_lshrrev_b32_e32 v41, 8, v0
	v_add_u32_e32 v44, 0x2410, v5
	v_lshlrev_b32_e32 v5, 3, v4
	v_lshl_or_b32 v5, v41, 12, v5
	v_add_u32_e32 v5, 0, v5
	v_add_u32_e32 v45, 0x4410, v5
	v_and_b32_e32 v5, 32, v0
	v_lshl_or_b32 v4, v4, 6, v5
	v_lshl_add_u32 v28, v0, 3, 0
	v_lshlrev_b32_e32 v30, 2, v0
	s_lshl_b32 s36, s4, 9
	v_add_u32_e32 v4, 0, v4
	s_mov_b64 s[0:1], 0x41766408
	v_cmp_gt_u32_e64 s[6:7], 64, v0
	s_mov_b32 s21, 0
	v_lshl_add_u32 v29, v202, 3, 0
	v_sub_u32_e32 v31, v28, v30
	v_lshl_add_u32 v32, v66, 2, 0
	v_bfe_u32 v33, v0, 4, 1
	s_movk_i32 s30, 0x1f8
	v_or_b32_e32 v38, 0xfffffe00, v0
	s_add_i32 s31, s28, 64
	v_xor_b32_e32 v39, 63, v1
	v_lshrrev_b32_e32 v40, 2, v0
	s_nop 0
	v_lshrrev_b32_e32 v42, 3, v0
	v_lshlrev_b32_e32 v43, 6, v0
	v_add_u32_e32 v46, 0x8410, v4
	v_lshl_add_u64 v[16:17], v[2:3], 0, s[0:1]
	s_mov_b32 s37, 0x3fb8aa3b
	s_mov_b32 s38, 0xc2ce8ed0
	s_mov_b32 s39, 0x42b17218
	v_mov_b32_e32 v47, 0x7f800000
	s_brev_b32 s40, 18
	s_mov_b32 s41, 0xfe5163ab
	s_mov_b32 s42, 0x3c439041
	s_mov_b32 s43, 0xdb629599
	s_mov_b32 s44, 0xf534ddc0
	s_mov_b32 s45, 0xfc2757d1
	s_mov_b32 s46, 0x4e441529
	s_mov_b32 s47, 0xa2f9836e
	s_mov_b32 s48, 0x3fc90fda
	s_mov_b32 s49, 0x3f22f983
	s_mov_b32 s50, 0xbfc90fda
	v_mov_b32_e32 v48, 0x3c0881c4
	v_mov_b32_e32 v49, 0xbab64f3b
	s_brev_b32 s51, 1
	s_mov_b64 s[22:23], 0x800
	s_mov_b64 s[24:25], 0x2000
	s_movk_i32 s68, 0xdff
	v_not_b32_e32 v50, 63
	v_not_b32_e32 v51, 31
	v_mov_b32_e32 v52, 0x7fc00000
	v_readlane_b32 s13, v252, 20
